# in-proj GEMM loop: LDS-DMA pieces addressed as SGPR base + 32-bit lane offset (16 v_lshl_add_u64 per trip removed)
# speedup vs baseline: 1.0016x; 1.0004x over previous
.LBB0_213:
	s_add_u32 s14, s12, 0xfffc0080
	s_addc_u32 s15, s13, -1
	s_add_i32 s36, 0, 0x10000
	s_cmp_eq_u32 s29, 12
	s_cselect_b32 s17, s9, s15
	s_cselect_b32 s16, s8, s14
	s_cselect_b32 s15, s11, s28
	s_cselect_b32 s14, s10, s7
	s_add_i32 s42, 0, 0x14000
	v_add_u32_e32 v158, s36, v147
	v_add_u32_e32 v174, s42, v147
	ds_read_b128 v[142:145], v158
	ds_read_b128 v[150:153], v158 offset:1024
	ds_read_b128 v[154:157], v158 offset:2048
	ds_read_b128 v[158:161], v158 offset:3072
	ds_read_b128 v[162:165], v174
	ds_read_b128 v[166:169], v174 offset:1024
	ds_read_b128 v[170:173], v174 offset:2048
	ds_read_b128 v[174:177], v174 offset:3072
	s_add_i32 m0, s19, 0xc000
	ds_read_b128 v[178:181], v149
	ds_read_b128 v[182:185], v149 offset:1024
	ds_read_b128 v[186:189], v149 offset:2048
	ds_read_b128 v[198:201], v149 offset:3072
	ds_read_b128 v[202:205], v149 offset:4096
	ds_read_b128 v[206:209], v149 offset:5120
	ds_read_b128 v[210:213], v149 offset:6144
	ds_read_b128 v[214:217], v149 offset:7168
	global_load_lds_dwordx4 v138, s[12:13]
	s_add_i32 m0, s19, 0xe000
	s_nop 0
	global_load_lds_dwordx4 v140, s[12:13]
	s_waitcnt vmcnt(8)
	s_waitcnt lgkmcnt(0)
	s_barrier
	s_setprio 1
	s_waitcnt lgkmcnt(0)
	v_mfma_f32_16x16x32_bf16 v[126:129], v[142:145], v[178:181], v[126:129]
	v_mfma_f32_16x16x32_bf16 v[122:125], v[154:157], v[178:181], v[122:125]
	v_mfma_f32_16x16x32_bf16 v[110:113], v[142:145], v[186:189], v[110:113]
	v_mfma_f32_16x16x32_bf16 v[106:109], v[154:157], v[186:189], v[106:109]
	v_mfma_f32_16x16x32_bf16 v[94:97], v[142:145], v[202:205], v[94:97]
	v_mfma_f32_16x16x32_bf16 v[90:93], v[154:157], v[202:205], v[90:93]
	v_mfma_f32_16x16x32_bf16 v[78:81], v[142:145], v[210:213], v[78:81]
	v_mfma_f32_16x16x32_bf16 v[74:77], v[154:157], v[210:213], v[74:77]
	v_mfma_f32_16x16x32_bf16 v[126:129], v[150:153], v[182:185], v[126:129]
	v_mfma_f32_16x16x32_bf16 v[122:125], v[158:161], v[182:185], v[122:125]
	v_mfma_f32_16x16x32_bf16 v[110:113], v[150:153], v[198:201], v[110:113]
	v_mfma_f32_16x16x32_bf16 v[106:109], v[158:161], v[198:201], v[106:109]
	v_mfma_f32_16x16x32_bf16 v[94:97], v[150:153], v[206:209], v[94:97]
	v_mfma_f32_16x16x32_bf16 v[90:93], v[158:161], v[206:209], v[90:93]
	v_mfma_f32_16x16x32_bf16 v[78:81], v[150:153], v[214:217], v[78:81]
	v_mfma_f32_16x16x32_bf16 v[74:77], v[158:161], v[214:217], v[74:77]
	s_setprio 0
	s_setprio 1
	v_mfma_f32_16x16x32_bf16 v[118:121], v[162:165], v[178:181], v[118:121]
	v_mfma_f32_16x16x32_bf16 v[114:117], v[170:173], v[178:181], v[114:117]
	v_mfma_f32_16x16x32_bf16 v[102:105], v[162:165], v[186:189], v[102:105]
	v_mfma_f32_16x16x32_bf16 v[98:101], v[170:173], v[186:189], v[98:101]
	v_mfma_f32_16x16x32_bf16 v[86:89], v[162:165], v[202:205], v[86:89]
	v_mfma_f32_16x16x32_bf16 v[82:85], v[170:173], v[202:205], v[82:85]
	v_mfma_f32_16x16x32_bf16 v[70:73], v[162:165], v[210:213], v[70:73]
	v_mfma_f32_16x16x32_bf16 v[66:69], v[170:173], v[210:213], v[66:69]
	v_mfma_f32_16x16x32_bf16 v[118:121], v[166:169], v[182:185], v[118:121]
	v_mfma_f32_16x16x32_bf16 v[114:117], v[174:177], v[182:185], v[114:117]
	v_mfma_f32_16x16x32_bf16 v[102:105], v[166:169], v[198:201], v[102:105]
	v_mfma_f32_16x16x32_bf16 v[98:101], v[174:177], v[198:201], v[98:101]
	v_mfma_f32_16x16x32_bf16 v[86:89], v[166:169], v[206:209], v[86:89]
	v_mfma_f32_16x16x32_bf16 v[82:85], v[174:177], v[206:209], v[82:85]
	v_mfma_f32_16x16x32_bf16 v[70:73], v[166:169], v[214:217], v[70:73]
	v_mfma_f32_16x16x32_bf16 v[66:69], v[174:177], v[214:217], v[66:69]
	s_setprio 0
	s_barrier
	s_add_i32 s36, s36, s18
	s_mov_b32 m0, s36
	ds_read_b128 v[178:181], v149 offset:16384
	ds_read_b128 v[182:185], v149 offset:17408
	ds_read_b128 v[186:189], v149 offset:18432
	ds_read_b128 v[198:201], v149 offset:19456
	ds_read_b128 v[202:205], v149 offset:20480
	ds_read_b128 v[206:209], v149 offset:21504
	ds_read_b128 v[210:213], v149 offset:22528
	ds_read_b128 v[214:217], v149 offset:23552
	global_load_lds_dwordx4 v130, s[14:15]
	s_add_i32 m0, s36, 0x2000
	s_add_u32 s36, s14, 0x40000
	s_addc_u32 s37, s15, 0
	s_add_i32 s42, s42, s18
	global_load_lds_dwordx4 v132, s[14:15]
	s_mov_b32 m0, s42
	s_add_u32 s98, s16, s84
	s_addc_u32 s99, s17, s85
	global_load_lds_dwordx4 v130, s[36:37]
	s_add_i32 m0, s42, 0x2000
	s_nop 0
	global_load_lds_dwordx4 v132, s[36:37]
	s_mov_b32 m0, s19
	s_nop 0
	global_load_lds_dwordx4 v136, s[16:17]
	s_mov_b32 m0, s20
	s_nop 0
	global_load_lds_dwordx4 v134, s[16:17]
	s_waitcnt vmcnt(8)
	s_waitcnt lgkmcnt(0)
	s_barrier
	s_setprio 1
	s_waitcnt lgkmcnt(0)
	v_mfma_f32_16x16x32_bf16 v[62:65], v[142:145], v[178:181], v[62:65]
	v_mfma_f32_16x16x32_bf16 v[58:61], v[154:157], v[178:181], v[58:61]
	v_mfma_f32_16x16x32_bf16 v[46:49], v[142:145], v[186:189], v[46:49]
	v_mfma_f32_16x16x32_bf16 v[42:45], v[154:157], v[186:189], v[42:45]
	v_mfma_f32_16x16x32_bf16 v[30:33], v[142:145], v[202:205], v[30:33]
	v_mfma_f32_16x16x32_bf16 v[26:29], v[154:157], v[202:205], v[26:29]
	v_mfma_f32_16x16x32_bf16 v[14:17], v[142:145], v[210:213], v[14:17]
	v_mfma_f32_16x16x32_bf16 v[10:13], v[154:157], v[210:213], v[10:13]
	v_mfma_f32_16x16x32_bf16 v[62:65], v[150:153], v[182:185], v[62:65]
	v_mfma_f32_16x16x32_bf16 v[58:61], v[158:161], v[182:185], v[58:61]
	v_mfma_f32_16x16x32_bf16 v[46:49], v[150:153], v[198:201], v[46:49]
	v_mfma_f32_16x16x32_bf16 v[42:45], v[158:161], v[198:201], v[42:45]
	v_mfma_f32_16x16x32_bf16 v[30:33], v[150:153], v[206:209], v[30:33]
	v_mfma_f32_16x16x32_bf16 v[26:29], v[158:161], v[206:209], v[26:29]
	v_mfma_f32_16x16x32_bf16 v[14:17], v[150:153], v[214:217], v[14:17]
	v_mfma_f32_16x16x32_bf16 v[10:13], v[158:161], v[214:217], v[10:13]
	s_setprio 0
	s_setprio 1
	v_mfma_f32_16x16x32_bf16 v[54:57], v[162:165], v[178:181], v[54:57]
	v_mfma_f32_16x16x32_bf16 v[50:53], v[170:173], v[178:181], v[50:53]
	v_mfma_f32_16x16x32_bf16 v[38:41], v[162:165], v[186:189], v[38:41]
	v_mfma_f32_16x16x32_bf16 v[34:37], v[170:173], v[186:189], v[34:37]
	v_mfma_f32_16x16x32_bf16 v[22:25], v[162:165], v[202:205], v[22:25]
	v_mfma_f32_16x16x32_bf16 v[18:21], v[170:173], v[202:205], v[18:21]
	v_mfma_f32_16x16x32_bf16 v[6:9], v[162:165], v[210:213], v[6:9]
	v_mfma_f32_16x16x32_bf16 v[2:5], v[170:173], v[210:213], v[2:5]
	v_mfma_f32_16x16x32_bf16 v[54:57], v[166:169], v[182:185], v[54:57]
	v_mfma_f32_16x16x32_bf16 v[50:53], v[174:177], v[182:185], v[50:53]
	v_mfma_f32_16x16x32_bf16 v[38:41], v[166:169], v[198:201], v[38:41]
	v_mfma_f32_16x16x32_bf16 v[34:37], v[174:177], v[198:201], v[34:37]
	v_mfma_f32_16x16x32_bf16 v[22:25], v[166:169], v[206:209], v[22:25]
	v_mfma_f32_16x16x32_bf16 v[18:21], v[174:177], v[206:209], v[18:21]
	v_mfma_f32_16x16x32_bf16 v[6:9], v[166:169], v[214:217], v[6:9]
	v_mfma_f32_16x16x32_bf16 v[2:5], v[174:177], v[214:217], v[2:5]
	s_setprio 0
	s_barrier
	s_add_i32 s36, 0, 0x18000
	s_add_i32 s37, 0, 0x1c000
	v_add_u32_e32 v158, s36, v147
	v_add_u32_e32 v174, s37, v147
	ds_read_b128 v[142:145], v158
	ds_read_b128 v[150:153], v158 offset:1024
	ds_read_b128 v[154:157], v158 offset:2048
	ds_read_b128 v[158:161], v158 offset:3072
	ds_read_b128 v[162:165], v174
	ds_read_b128 v[166:169], v174 offset:1024
	ds_read_b128 v[170:173], v174 offset:2048
	ds_read_b128 v[174:177], v174 offset:3072
	s_add_u32 s16, s16, 0x40000
	s_addc_u32 s17, s17, 0
	s_mov_b32 m0, s21
	ds_read_b128 v[178:181], v149 offset:32768
	ds_read_b128 v[182:185], v149 offset:33792
	ds_read_b128 v[186:189], v149 offset:34816
	ds_read_b128 v[198:201], v149 offset:35840
	ds_read_b128 v[202:205], v149 offset:36864
	ds_read_b128 v[206:209], v149 offset:37888
	ds_read_b128 v[210:213], v149 offset:38912
	ds_read_b128 v[214:217], v149 offset:39936
	global_load_lds_dwordx4 v136, s[16:17]
	s_mov_b32 m0, s22
	s_nop 0
	global_load_lds_dwordx4 v134, s[16:17]
	s_waitcnt vmcnt(8)
	s_waitcnt lgkmcnt(0)
	s_barrier
	s_setprio 1
	s_waitcnt lgkmcnt(0)
	v_mfma_f32_16x16x32_bf16 v[126:129], v[142:145], v[178:181], v[126:129]
	v_mfma_f32_16x16x32_bf16 v[122:125], v[154:157], v[178:181], v[122:125]
	v_mfma_f32_16x16x32_bf16 v[110:113], v[142:145], v[186:189], v[110:113]
	v_mfma_f32_16x16x32_bf16 v[106:109], v[154:157], v[186:189], v[106:109]
	v_mfma_f32_16x16x32_bf16 v[94:97], v[142:145], v[202:205], v[94:97]
	v_mfma_f32_16x16x32_bf16 v[90:93], v[154:157], v[202:205], v[90:93]
	v_mfma_f32_16x16x32_bf16 v[78:81], v[142:145], v[210:213], v[78:81]
	v_mfma_f32_16x16x32_bf16 v[74:77], v[154:157], v[210:213], v[74:77]
	v_mfma_f32_16x16x32_bf16 v[126:129], v[150:153], v[182:185], v[126:129]
	v_mfma_f32_16x16x32_bf16 v[122:125], v[158:161], v[182:185], v[122:125]
	v_mfma_f32_16x16x32_bf16 v[110:113], v[150:153], v[198:201], v[110:113]
	v_mfma_f32_16x16x32_bf16 v[106:109], v[158:161], v[198:201], v[106:109]
	v_mfma_f32_16x16x32_bf16 v[94:97], v[150:153], v[206:209], v[94:97]
	v_mfma_f32_16x16x32_bf16 v[90:93], v[158:161], v[206:209], v[90:93]
	v_mfma_f32_16x16x32_bf16 v[78:81], v[150:153], v[214:217], v[78:81]
	v_mfma_f32_16x16x32_bf16 v[74:77], v[158:161], v[214:217], v[74:77]
	s_setprio 0
	s_setprio 1
	v_mfma_f32_16x16x32_bf16 v[118:121], v[162:165], v[178:181], v[118:121]
	v_mfma_f32_16x16x32_bf16 v[114:117], v[170:173], v[178:181], v[114:117]
	v_mfma_f32_16x16x32_bf16 v[102:105], v[162:165], v[186:189], v[102:105]
	v_mfma_f32_16x16x32_bf16 v[98:101], v[170:173], v[186:189], v[98:101]
	v_mfma_f32_16x16x32_bf16 v[86:89], v[162:165], v[202:205], v[86:89]
	v_mfma_f32_16x16x32_bf16 v[82:85], v[170:173], v[202:205], v[82:85]
	v_mfma_f32_16x16x32_bf16 v[70:73], v[162:165], v[210:213], v[70:73]
	v_mfma_f32_16x16x32_bf16 v[66:69], v[170:173], v[210:213], v[66:69]
	v_mfma_f32_16x16x32_bf16 v[118:121], v[166:169], v[182:185], v[118:121]
	v_mfma_f32_16x16x32_bf16 v[114:117], v[174:177], v[182:185], v[114:117]
	v_mfma_f32_16x16x32_bf16 v[102:105], v[166:169], v[198:201], v[102:105]
	v_mfma_f32_16x16x32_bf16 v[98:101], v[174:177], v[198:201], v[98:101]
	v_mfma_f32_16x16x32_bf16 v[86:89], v[166:169], v[206:209], v[86:89]
	v_mfma_f32_16x16x32_bf16 v[82:85], v[174:177], v[206:209], v[82:85]
	v_mfma_f32_16x16x32_bf16 v[70:73], v[166:169], v[214:217], v[70:73]
	v_mfma_f32_16x16x32_bf16 v[66:69], v[174:177], v[214:217], v[66:69]
	s_setprio 0
	s_barrier
	s_add_i32 s16, s36, s18
	s_add_u32 s100, s14, s84
	s_addc_u32 s101, s15, s85
	s_mov_b32 m0, s16
	ds_read_b128 v[178:181], v149 offset:49152
	ds_read_b128 v[182:185], v149 offset:50176
	ds_read_b128 v[186:189], v149 offset:51200
	ds_read_b128 v[198:201], v149 offset:52224
	ds_read_b128 v[202:205], v149 offset:53248
	ds_read_b128 v[206:209], v149 offset:54272
	ds_read_b128 v[210:213], v149 offset:55296
	ds_read_b128 v[214:217], v149 offset:56320
	global_load_lds_dwordx4 v130, s[100:101]
	s_add_i32 m0, s16, 0x2000
	s_add_u32 s14, s14, 0x40080
	s_addc_u32 s15, s15, 0
	s_add_i32 s16, s37, s18
	global_load_lds_dwordx4 v132, s[100:101]
	s_mov_b32 m0, s16
	s_nop 0
	global_load_lds_dwordx4 v130, s[14:15]
	s_add_i32 m0, s16, 0x2000
	s_nop 0
	global_load_lds_dwordx4 v132, s[14:15]
	s_mov_b32 m0, s23
	s_nop 0
	global_load_lds_dwordx4 v136, s[98:99]
	s_mov_b32 m0, s24
	s_nop 0
	global_load_lds_dwordx4 v134, s[98:99]
	s_waitcnt vmcnt(8)
	s_waitcnt lgkmcnt(0)
	s_barrier
	s_setprio 1
	s_waitcnt lgkmcnt(0)
	v_mfma_f32_16x16x32_bf16 v[62:65], v[142:145], v[178:181], v[62:65]
	v_mfma_f32_16x16x32_bf16 v[58:61], v[154:157], v[178:181], v[58:61]
	v_mfma_f32_16x16x32_bf16 v[46:49], v[142:145], v[186:189], v[46:49]
	v_mfma_f32_16x16x32_bf16 v[42:45], v[154:157], v[186:189], v[42:45]
	v_mfma_f32_16x16x32_bf16 v[30:33], v[142:145], v[202:205], v[30:33]
	v_mfma_f32_16x16x32_bf16 v[26:29], v[154:157], v[202:205], v[26:29]
	v_mfma_f32_16x16x32_bf16 v[14:17], v[142:145], v[210:213], v[14:17]
	v_mfma_f32_16x16x32_bf16 v[10:13], v[154:157], v[210:213], v[10:13]
	v_mfma_f32_16x16x32_bf16 v[62:65], v[150:153], v[182:185], v[62:65]
	v_mfma_f32_16x16x32_bf16 v[58:61], v[158:161], v[182:185], v[58:61]
	v_mfma_f32_16x16x32_bf16 v[46:49], v[150:153], v[198:201], v[46:49]
	v_mfma_f32_16x16x32_bf16 v[42:45], v[158:161], v[198:201], v[42:45]
	v_mfma_f32_16x16x32_bf16 v[30:33], v[150:153], v[206:209], v[30:33]
	v_mfma_f32_16x16x32_bf16 v[26:29], v[158:161], v[206:209], v[26:29]
	v_mfma_f32_16x16x32_bf16 v[14:17], v[150:153], v[214:217], v[14:17]
	v_mfma_f32_16x16x32_bf16 v[10:13], v[158:161], v[214:217], v[10:13]
	s_setprio 0
	s_setprio 1
	v_mfma_f32_16x16x32_bf16 v[54:57], v[162:165], v[178:181], v[54:57]
	v_mfma_f32_16x16x32_bf16 v[50:53], v[170:173], v[178:181], v[50:53]
	v_mfma_f32_16x16x32_bf16 v[38:41], v[162:165], v[186:189], v[38:41]
	v_mfma_f32_16x16x32_bf16 v[34:37], v[170:173], v[186:189], v[34:37]
	v_mfma_f32_16x16x32_bf16 v[22:25], v[162:165], v[202:205], v[22:25]
	v_mfma_f32_16x16x32_bf16 v[18:21], v[170:173], v[202:205], v[18:21]
	v_mfma_f32_16x16x32_bf16 v[6:9], v[162:165], v[210:213], v[6:9]
	v_mfma_f32_16x16x32_bf16 v[2:5], v[170:173], v[210:213], v[2:5]
	v_mfma_f32_16x16x32_bf16 v[54:57], v[166:169], v[182:185], v[54:57]
	v_mfma_f32_16x16x32_bf16 v[50:53], v[174:177], v[182:185], v[50:53]
	v_mfma_f32_16x16x32_bf16 v[38:41], v[166:169], v[198:201], v[38:41]
	v_mfma_f32_16x16x32_bf16 v[34:37], v[174:177], v[198:201], v[34:37]
	v_mfma_f32_16x16x32_bf16 v[22:25], v[166:169], v[206:209], v[22:25]
	v_mfma_f32_16x16x32_bf16 v[18:21], v[174:177], v[206:209], v[18:21]
	v_mfma_f32_16x16x32_bf16 v[6:9], v[166:169], v[214:217], v[6:9]
	v_mfma_f32_16x16x32_bf16 v[2:5], v[174:177], v[214:217], v[2:5]
	s_setprio 0
	s_barrier
	s_add_i32 s29, s29, 2
	s_add_u32 s12, s12, 0x100
	s_addc_u32 s13, s13, 0
	s_add_u32 s7, s7, 0x100
	s_addc_u32 s28, s28, 0
	s_cmp_gt_u32 s29, 13
	s_cbranch_scc0 .LBB0_213
	s_and_b64 vcc, exec, s[4:5]
	s_cbranch_vccz .LBB0_216
	s_barrier
